# RWKV scan serial chain (sec 7.2/7.12): each step's LDS wait + progress publish deferred past the step's first MFMA pair, SCC-safe exec switch
# baseline (speedup 1.0000x reference)
.LBB0_1305:
	s_lshl_b32 s2, s18, 11
	s_and_b32 s2, s2, 0x3000
	v_add_u32_e32 v202, s2, v177
	v_cvt_pk_bf16_f32 v162, v158, v159
	v_cvt_pk_bf16_f32 v163, v160, v161
	v_cvt_pk_bf16_f32 v164, v154, v155
	v_cvt_pk_bf16_f32 v165, v156, v157
	v_cvt_pk_bf16_f32 v166, v150, v151
	v_cvt_pk_bf16_f32 v167, v152, v153
	v_cvt_pk_bf16_f32 v168, v106, v107
	v_cvt_pk_bf16_f32 v169, v108, v109
	ds_write2st64_b64 v202, v[162:163], v[164:165] offset1:1
	ds_write2st64_b64 v202, v[166:167], v[168:169] offset0:2 offset1:3
	s_nop 1
	s_or_b32 s24, s18, 1
	v_mov_b32_e32 v222, s12
	v_add_u32_e32 v222, 0x10000, v222
	v_mov_b32_e32 v223, s24
	s_waitcnt vmcnt(45)
	v_lshlrev_b32_e32 v202, 16, v188
	v_and_b32_e32 v203, 0xffff0000, v188
	s_waitcnt vmcnt(44)
	v_pk_fma_f32 v[46:47], v[158:159], v[46:47], v[202:203]
	v_lshlrev_b32_e32 v158, 16, v189
	v_and_b32_e32 v159, 0xffff0000, v189
	v_pk_fma_f32 v[48:49], v[160:161], v[48:49], v[158:159]
	s_sub_i32 s2, 0x7c, s18
	s_add_i32 s10, s18, 3
	v_mfma_f32_16x16x32_bf16 v[38:41], v[38:41], v[162:165], v[46:49]
	s_and_b64 s[26:27], s[6:7], exec
	s_cselect_b32 s2, s10, s2
	s_add_i32 s26, s2, s19
	v_mfma_f32_16x16x32_bf16 v[158:161], v[30:33], v[166:169], v[38:41]
	s_waitcnt lgkmcnt(0)
	s_mov_b64 s[98:99], exec
	s_mov_b64 exec, s[0:1]
	ds_write_b32 v222, v223
	s_mov_b64 exec, s[98:99]
	s_waitcnt vmcnt(41)
	v_lshlrev_b32_e32 v30, 16, v186
	v_and_b32_e32 v31, 0xffff0000, v186
	v_lshlrev_b32_e32 v32, 16, v187
	v_and_b32_e32 v33, 0xffff0000, v187
	s_waitcnt vmcnt(40)
	v_pk_fma_f32 v[30:31], v[154:155], v[42:43], v[30:31]
	v_pk_fma_f32 v[32:33], v[156:157], v[44:45], v[32:33]
	s_ashr_i32 s27, s26, 31
	s_lshl_b64 s[28:29], s[26:27], 13
	v_mfma_f32_16x16x32_bf16 v[18:21], v[18:21], v[162:165], v[30:33]
	s_add_u32 s30, s20, s28
	s_addc_u32 s31, s21, s29
	s_lshl_b64 s[26:27], s[26:27], 8
	v_mfma_f32_16x16x32_bf16 v[154:157], v[22:25], v[166:169], v[18:21]
	v_lshl_add_u64 v[30:31], v[178:179], 0, s[26:27]
	v_lshl_add_u64 v[32:33], v[180:181], 0, s[28:29]
	s_waitcnt vmcnt(37)
	s_nop 0
	v_lshlrev_b32_e32 v18, 16, v182
	v_and_b32_e32 v19, 0xffff0000, v182
	v_lshlrev_b32_e32 v20, 16, v183
	v_and_b32_e32 v21, 0xffff0000, v183
	s_waitcnt vmcnt(36)
	v_pk_fma_f32 v[18:19], v[150:151], v[26:27], v[18:19]
	v_pk_fma_f32 v[20:21], v[152:153], v[28:29], v[20:21]
	s_nop 1
	v_mfma_f32_16x16x32_bf16 v[2:5], v[2:5], v[162:165], v[18:21]
	v_mfma_f32_16x16x32_bf16 v[150:153], v[14:17], v[166:169], v[2:5]
	s_waitcnt vmcnt(33)
	s_nop 5
	v_lshlrev_b32_e32 v2, 16, v184
	v_and_b32_e32 v3, 0xffff0000, v184
	v_lshlrev_b32_e32 v4, 16, v185
	v_and_b32_e32 v5, 0xffff0000, v185
	s_waitcnt vmcnt(32)
	v_pk_fma_f32 v[2:3], v[106:107], v[34:35], v[2:3]
	v_pk_fma_f32 v[4:5], v[108:109], v[36:37], v[4:5]
	global_load_dwordx4 v[42:45], v174, s[30:31]
	global_load_dwordx4 v[34:37], v174, s[30:31] offset:1024
	v_mfma_f32_16x16x32_bf16 v[2:5], v[6:9], v[162:165], v[2:5]
	v_lshl_add_u64 v[6:7], s[30:31], 0, v[174:175]
	v_mfma_f32_16x16x32_bf16 v[106:109], v[10:13], v[166:169], v[2:5]
	v_add_co_u32_e32 v10, vcc, 0x1000, v6
	global_load_dwordx2 v[188:189], v[32:33], off
	global_load_dwordx4 v[46:49], v[30:31], off
	global_load_dwordx4 v[18:21], v174, s[30:31] offset:2048
	global_load_dwordx4 v[22:25], v174, s[30:31] offset:3072
	global_load_dwordx2 v[186:187], v[32:33], off offset:512
	global_load_dwordx4 v[38:41], v[30:31], off offset:64
	global_load_dwordx4 v[2:5], v206, s[30:31]
	v_addc_co_u32_e32 v11, vcc, 0, v7, vcc
	global_load_dwordx4 v[14:17], v[10:11], off offset:1024
	global_load_dwordx2 v[182:183], v[32:33], off offset:1024
	global_load_dwordx4 v[26:29], v[30:31], off offset:128
	global_load_dwordx4 v[6:9], v207, s[30:31]
	s_nop 0
	global_load_dwordx4 v[10:13], v[10:11], off offset:3072
	s_nop 0
	global_load_dwordx2 v[184:185], v[32:33], off offset:1536
	s_nop 0
	global_load_dwordx4 v[30:33], v[30:31], off offset:192
	s_andn2_b64 vcc, exec, s[8:9]
	s_cbranch_vccnz .LBB0_1310
	s_add_i32 s8, s12, 0
	s_add_i32 s8, s8, 0x10020
	v_mov_b32_e32 v162, s8
	ds_read_b32 v162, v162
	s_waitcnt lgkmcnt(0)
	v_add_u32_e32 v162, 8, v162
	v_cmp_lt_u32_e32 vcc, s24, v162
	s_cbranch_vccnz .LBB0_1310

.LBB0_1310:
	s_lshl_b32 s2, s24, 11
	s_and_b32 s2, s2, 0x3800
	v_add_u32_e32 v202, s2, v177
	v_cvt_pk_bf16_f32 v162, v158, v159
	v_cvt_pk_bf16_f32 v163, v160, v161
	v_cvt_pk_bf16_f32 v164, v154, v155
	v_cvt_pk_bf16_f32 v165, v156, v157
	v_cvt_pk_bf16_f32 v166, v150, v151
	v_cvt_pk_bf16_f32 v167, v152, v153
	v_cvt_pk_bf16_f32 v168, v106, v107
	v_cvt_pk_bf16_f32 v169, v108, v109
	ds_write2st64_b64 v202, v[162:163], v[164:165] offset1:1
	ds_write2st64_b64 v202, v[166:167], v[168:169] offset0:2 offset1:3
	s_nop 1
	v_mov_b32_e32 v222, s12
	v_add_u32_e32 v222, 0x10000, v222
	v_mov_b32_e32 v223, s23
	s_waitcnt vmcnt(37)
	v_lshlrev_b32_e32 v202, 16, v196
	v_and_b32_e32 v203, 0xffff0000, v196
	s_waitcnt vmcnt(44)
	v_pk_fma_f32 v[94:95], v[94:95], v[158:159], v[202:203]
	v_lshlrev_b32_e32 v158, 16, v197
	v_and_b32_e32 v159, 0xffff0000, v197
	v_pk_fma_f32 v[96:97], v[96:97], v[160:161], v[158:159]
	s_sub_i32 s2, 0x7b, s18
	s_add_i32 s11, s18, 4
	v_mfma_f32_16x16x32_bf16 v[78:81], v[78:81], v[162:165], v[94:97]
	s_and_b64 s[8:9], s[6:7], exec
	s_cselect_b32 s2, s11, s2
	s_add_i32 s8, s2, s19
	v_mfma_f32_16x16x32_bf16 v[158:161], v[70:73], v[166:169], v[78:81]
	s_waitcnt lgkmcnt(0)
	s_mov_b64 s[98:99], exec
	s_mov_b64 exec, s[0:1]
	ds_write_b32 v222, v223
	s_mov_b64 exec, s[98:99]
	s_waitcnt vmcnt(36)
	v_lshlrev_b32_e32 v70, 16, v194
	v_and_b32_e32 v71, 0xffff0000, v194
	v_lshlrev_b32_e32 v72, 16, v195
	v_and_b32_e32 v73, 0xffff0000, v195
	s_waitcnt vmcnt(40)
	v_pk_fma_f32 v[70:71], v[82:83], v[154:155], v[70:71]
	v_pk_fma_f32 v[72:73], v[84:85], v[156:157], v[72:73]
	s_ashr_i32 s9, s8, 31
	s_lshl_b64 s[24:25], s[8:9], 13
	v_mfma_f32_16x16x32_bf16 v[50:53], v[50:53], v[162:165], v[70:73]
	s_add_u32 s26, s20, s24
	s_addc_u32 s27, s21, s25
	s_lshl_b64 s[8:9], s[8:9], 8
	v_mfma_f32_16x16x32_bf16 v[94:97], v[58:61], v[166:169], v[50:53]
	s_cmp_lt_u32 s18, 6
	s_waitcnt vmcnt(35)
	s_nop 1
	v_lshlrev_b32_e32 v50, 16, v190
	v_and_b32_e32 v51, 0xffff0000, v190
	v_lshlrev_b32_e32 v52, 16, v191
	v_and_b32_e32 v53, 0xffff0000, v191
	s_waitcnt vmcnt(33)
	v_pk_fma_f32 v[50:51], v[86:87], v[150:151], v[50:51]
	v_pk_fma_f32 v[52:53], v[88:89], v[152:153], v[52:53]
	global_load_dwordx4 v[86:89], v174, s[26:27]
	global_load_dwordx4 v[78:81], v174, s[26:27] offset:1024
	v_mfma_f32_16x16x32_bf16 v[50:53], v[54:57], v[162:165], v[50:53]
	v_lshl_add_u64 v[54:55], s[26:27], 0, v[174:175]
	v_mfma_f32_16x16x32_bf16 v[150:153], v[74:77], v[166:169], v[50:53]
	v_lshl_add_u64 v[74:75], v[178:179], 0, s[8:9]
	v_lshl_add_u64 v[76:77], v[180:181], 0, s[24:25]
	s_waitcnt vmcnt(35)
	s_nop 2
	v_lshlrev_b32_e32 v50, 16, v192
	v_and_b32_e32 v51, 0xffff0000, v192
	v_lshlrev_b32_e32 v52, 16, v193
	v_and_b32_e32 v53, 0xffff0000, v193
	s_waitcnt vmcnt(34)
	v_pk_fma_f32 v[50:51], v[90:91], v[106:107], v[50:51]
	v_pk_fma_f32 v[52:53], v[92:93], v[108:109], v[52:53]
	v_add_co_u32_e32 v106, vcc, 0x1000, v54
	s_nop 0
	v_mfma_f32_16x16x32_bf16 v[50:53], v[62:65], v[162:165], v[50:53]
	v_addc_co_u32_e32 v107, vcc, 0, v55, vcc
	v_mfma_f32_16x16x32_bf16 v[154:157], v[66:69], v[166:169], v[50:53]
	global_load_dwordx2 v[196:197], v[76:77], off
	global_load_dwordx4 v[90:93], v[74:75], off
	global_load_dwordx4 v[62:65], v174, s[26:27] offset:2048
	global_load_dwordx4 v[66:69], v174, s[26:27] offset:3072
	global_load_dwordx2 v[194:195], v[76:77], off offset:512
	global_load_dwordx4 v[82:85], v[74:75], off offset:64
	global_load_dwordx4 v[50:53], v206, s[26:27]
	global_load_dwordx4 v[58:61], v[106:107], off offset:1024
	global_load_dwordx2 v[190:191], v[76:77], off offset:1024
	global_load_dwordx4 v[70:73], v[74:75], off offset:128
	global_load_dwordx4 v[54:57], v207, s[26:27]
	s_nop 0
	global_load_dwordx4 v[106:109], v[106:107], off offset:3072
	s_nop 0
	global_load_dwordx2 v[192:193], v[76:77], off offset:1536
	s_nop 0
	global_load_dwordx4 v[74:77], v[74:75], off offset:192
	s_cbranch_scc1 .LBB0_1315
	s_add_i32 s8, s12, 0
	s_add_i32 s8, s8, 0x10020
	v_mov_b32_e32 v162, s8
	ds_read_b32 v162, v162
	s_waitcnt lgkmcnt(0)
	v_add_u32_e32 v162, 8, v162
	v_cmp_lt_u32_e32 vcc, s23, v162
	s_cbranch_vccnz .LBB0_1315

.LBB0_1315:
	s_lshl_b32 s2, s23, 11
	s_and_b32 s2, s2, 0x3000
	v_add_u32_e32 v202, s2, v177
	v_cvt_pk_bf16_f32 v162, v158, v159
	v_cvt_pk_bf16_f32 v163, v160, v161
	v_cvt_pk_bf16_f32 v164, v94, v95
	v_cvt_pk_bf16_f32 v165, v96, v97
	v_cvt_pk_bf16_f32 v166, v150, v151
	v_cvt_pk_bf16_f32 v167, v152, v153
	v_cvt_pk_bf16_f32 v168, v154, v155
	v_cvt_pk_bf16_f32 v169, v156, v157
	ds_write2st64_b64 v202, v[162:163], v[164:165] offset1:1
	ds_write2st64_b64 v202, v[166:167], v[168:169] offset0:2 offset1:3
	s_nop 1
	v_mov_b32_e32 v222, s12
	v_add_u32_e32 v222, 0x10000, v222
	v_mov_b32_e32 v223, s10
	s_waitcnt vmcnt(37)
	v_lshlrev_b32_e32 v202, 16, v200
	v_and_b32_e32 v203, 0xffff0000, v200
	v_pk_fma_f32 v[146:147], v[146:147], v[158:159], v[202:203]
	v_lshlrev_b32_e32 v158, 16, v201
	v_and_b32_e32 v159, 0xffff0000, v201
	v_pk_fma_f32 v[148:149], v[148:149], v[160:161], v[158:159]
	s_sub_i32 s2, 0x7a, s18
	s_add_i32 s23, s18, 5
	v_mfma_f32_16x16x32_bf16 v[142:145], v[142:145], v[162:165], v[146:149]
	s_and_b64 s[8:9], s[6:7], exec
	s_cselect_b32 s2, s23, s2
	s_add_i32 s8, s2, s19
	v_mfma_f32_16x16x32_bf16 v[158:161], v[138:141], v[166:169], v[142:145]
	s_waitcnt lgkmcnt(0)
	s_mov_b64 s[98:99], exec
	s_mov_b64 exec, s[0:1]
	ds_write_b32 v222, v223
	s_mov_b64 exec, s[98:99]
	s_waitcnt vmcnt(36)
	v_lshlrev_b32_e32 v138, 16, v198
	v_and_b32_e32 v139, 0xffff0000, v198
	v_pk_fma_f32 v[94:95], v[134:135], v[94:95], v[138:139]
	v_lshlrev_b32_e32 v134, 16, v199
	v_and_b32_e32 v135, 0xffff0000, v199
	v_pk_fma_f32 v[96:97], v[136:137], v[96:97], v[134:135]
	s_ashr_i32 s9, s8, 31
	s_lshl_b64 s[24:25], s[8:9], 13
	v_mfma_f32_16x16x32_bf16 v[94:97], v[122:125], v[162:165], v[94:97]
	s_waitcnt vmcnt(35)
	v_lshlrev_b32_e32 v122, 16, v172
	v_and_b32_e32 v123, 0xffff0000, v172
	v_lshlrev_b32_e32 v124, 16, v173
	v_and_b32_e32 v125, 0xffff0000, v173
	s_waitcnt vmcnt(33)
	v_pk_fma_f32 v[122:123], v[130:131], v[150:151], v[122:123]
	v_pk_fma_f32 v[124:125], v[132:133], v[152:153], v[124:125]
	s_add_u32 s26, s20, s24
	s_addc_u32 s27, s21, s25
	v_mfma_f32_16x16x32_bf16 v[114:117], v[114:117], v[162:165], v[122:125]
	s_lshl_b64 s[8:9], s[8:9], 8
	v_lshl_add_u64 v[130:131], v[178:179], 0, s[8:9]
	v_lshl_add_u64 v[132:133], v[180:181], 0, s[24:25]
	v_mfma_f32_16x16x32_bf16 v[150:153], v[118:121], v[166:169], v[114:117]
	global_load_dwordx4 v[142:145], v174, s[26:27]
	global_load_dwordx4 v[134:137], v174, s[26:27] offset:1024
	s_cmp_lt_u32 s18, 5
	s_nop 0
	v_lshlrev_b32_e32 v114, 16, v170
	v_and_b32_e32 v115, 0xffff0000, v170
	s_waitcnt vmcnt(34)
	v_pk_fma_f32 v[110:111], v[110:111], v[154:155], v[114:115]
	v_lshlrev_b32_e32 v114, 16, v171
	v_and_b32_e32 v115, 0xffff0000, v171
	v_pk_fma_f32 v[112:113], v[112:113], v[156:157], v[114:115]
	v_mfma_f32_16x16x32_bf16 v[94:97], v[126:129], v[166:169], v[94:97]
	s_nop 0
	v_mfma_f32_16x16x32_bf16 v[98:101], v[98:101], v[162:165], v[110:113]
	v_mfma_f32_16x16x32_bf16 v[154:157], v[102:105], v[166:169], v[98:101]
	global_load_dwordx2 v[204:205], v[132:133], off
	global_load_dwordx4 v[146:149], v[130:131], off
	global_load_dwordx4 v[118:121], v174, s[26:27] offset:2048
	global_load_dwordx4 v[122:125], v174, s[26:27] offset:3072
	global_load_dwordx2 v[202:203], v[132:133], off offset:512
	global_load_dwordx4 v[138:141], v[130:131], off offset:64
	global_load_dwordx4 v[102:105], v206, s[26:27]
	v_lshl_add_u64 v[98:99], s[26:27], 0, v[174:175]
	v_add_co_u32_e32 v98, vcc, 0x1000, v98
	s_nop 1
	v_addc_co_u32_e32 v99, vcc, 0, v99, vcc
	global_load_dwordx4 v[114:117], v[98:99], off offset:1024
	global_load_dwordx2 v[198:199], v[132:133], off offset:1024
	global_load_dwordx4 v[126:129], v[130:131], off offset:128
	global_load_dwordx4 v[110:113], v207, s[26:27]
	s_nop 0
	global_load_dwordx4 v[98:101], v[98:99], off offset:3072
	s_nop 0
	global_load_dwordx2 v[200:201], v[132:133], off offset:1536
	s_nop 0
	global_load_dwordx4 v[130:133], v[130:131], off offset:192
	s_cbranch_scc1 .LBB0_1320
	s_add_i32 s8, s12, 0
	s_add_i32 s8, s8, 0x10020
	v_mov_b32_e32 v162, s8
	ds_read_b32 v162, v162
	s_waitcnt lgkmcnt(0)
	v_add_u32_e32 v162, 8, v162
	v_cmp_lt_u32_e32 vcc, s10, v162
	s_cbranch_vccnz .LBB0_1320

.LBB0_1320:
	s_lshl_b32 s2, s10, 11
	s_and_b32 s2, s2, 0x3800
	v_add_u32_e32 v170, s2, v177
	v_cvt_pk_bf16_f32 v162, v158, v159
	v_cvt_pk_bf16_f32 v163, v160, v161
	v_cvt_pk_bf16_f32 v164, v94, v95
	v_cvt_pk_bf16_f32 v165, v96, v97
	v_cvt_pk_bf16_f32 v166, v150, v151
	v_cvt_pk_bf16_f32 v167, v152, v153
	v_cvt_pk_bf16_f32 v168, v154, v155
	v_cvt_pk_bf16_f32 v169, v156, v157
	ds_write2st64_b64 v170, v[162:163], v[164:165] offset1:1
	ds_write2st64_b64 v170, v[166:167], v[168:169] offset0:2 offset1:3
	s_nop 1
	v_mov_b32_e32 v222, s12
	v_add_u32_e32 v222, 0x10000, v222
	v_mov_b32_e32 v223, s11
	s_waitcnt vmcnt(45)
	v_lshlrev_b32_e32 v170, 16, v188
	v_and_b32_e32 v171, 0xffff0000, v188
	s_waitcnt vmcnt(44)
	v_pk_fma_f32 v[46:47], v[46:47], v[158:159], v[170:171]
	v_lshlrev_b32_e32 v158, 16, v189
	v_and_b32_e32 v159, 0xffff0000, v189
	v_pk_fma_f32 v[48:49], v[48:49], v[160:161], v[158:159]
	s_sub_i32 s2, 0x79, s18
	s_add_i32 s10, s18, 6
	v_mfma_f32_16x16x32_bf16 v[42:45], v[42:45], v[162:165], v[46:49]
	s_and_b64 s[8:9], s[6:7], exec
	s_cselect_b32 s2, s10, s2
	s_add_i32 s8, s2, s19
	v_mfma_f32_16x16x32_bf16 v[158:161], v[34:37], v[166:169], v[42:45]
	s_waitcnt lgkmcnt(0)
	s_mov_b64 s[98:99], exec
	s_mov_b64 exec, s[0:1]
	ds_write_b32 v222, v223
	s_mov_b64 exec, s[98:99]
	s_waitcnt vmcnt(41)
	v_lshlrev_b32_e32 v34, 16, v186
	v_and_b32_e32 v35, 0xffff0000, v186
	v_lshlrev_b32_e32 v36, 16, v187
	v_and_b32_e32 v37, 0xffff0000, v187
	s_waitcnt vmcnt(40)
	v_pk_fma_f32 v[34:35], v[38:39], v[94:95], v[34:35]
	v_pk_fma_f32 v[36:37], v[40:41], v[96:97], v[36:37]
	s_ashr_i32 s9, s8, 31
	s_lshl_b64 s[24:25], s[8:9], 13
	v_mfma_f32_16x16x32_bf16 v[18:21], v[18:21], v[162:165], v[34:37]
	s_add_u32 s26, s20, s24
	s_addc_u32 s27, s21, s25
	s_lshl_b64 s[8:9], s[8:9], 8
	v_mfma_f32_16x16x32_bf16 v[94:97], v[22:25], v[166:169], v[18:21]
	v_lshl_add_u64 v[34:35], v[178:179], 0, s[8:9]
	v_lshl_add_u64 v[36:37], v[180:181], 0, s[24:25]
	s_cmp_lt_u32 s18, 4
	s_waitcnt vmcnt(37)
	v_lshlrev_b32_e32 v18, 16, v182
	v_and_b32_e32 v19, 0xffff0000, v182
	v_lshlrev_b32_e32 v20, 16, v183
	v_and_b32_e32 v21, 0xffff0000, v183
	s_waitcnt vmcnt(36)
	v_pk_fma_f32 v[18:19], v[26:27], v[150:151], v[18:19]
	v_pk_fma_f32 v[20:21], v[28:29], v[152:153], v[20:21]
	s_nop 1
	v_mfma_f32_16x16x32_bf16 v[2:5], v[2:5], v[162:165], v[18:21]
	v_mfma_f32_16x16x32_bf16 v[150:153], v[14:17], v[166:169], v[2:5]
	s_waitcnt vmcnt(33)
	s_nop 5
	v_lshlrev_b32_e32 v2, 16, v184
	v_and_b32_e32 v3, 0xffff0000, v184
	v_lshlrev_b32_e32 v4, 16, v185
	v_and_b32_e32 v5, 0xffff0000, v185
	s_waitcnt vmcnt(32)
	v_pk_fma_f32 v[2:3], v[30:31], v[154:155], v[2:3]
	v_pk_fma_f32 v[4:5], v[32:33], v[156:157], v[4:5]
	global_load_dwordx4 v[38:41], v174, s[26:27]
	global_load_dwordx4 v[30:33], v174, s[26:27] offset:1024
	v_mfma_f32_16x16x32_bf16 v[2:5], v[6:9], v[162:165], v[2:5]
	v_lshl_add_u64 v[6:7], s[26:27], 0, v[174:175]
	v_mfma_f32_16x16x32_bf16 v[154:157], v[10:13], v[166:169], v[2:5]
	v_add_co_u32_e32 v10, vcc, 0x1000, v6
	global_load_dwordx2 v[188:189], v[36:37], off
	global_load_dwordx4 v[46:49], v[34:35], off
	global_load_dwordx4 v[18:21], v174, s[26:27] offset:2048
	global_load_dwordx4 v[22:25], v174, s[26:27] offset:3072
	global_load_dwordx2 v[186:187], v[36:37], off offset:512
	global_load_dwordx4 v[42:45], v[34:35], off offset:64
	global_load_dwordx4 v[2:5], v206, s[26:27]
	v_addc_co_u32_e32 v11, vcc, 0, v7, vcc
	global_load_dwordx4 v[14:17], v[10:11], off offset:1024
	global_load_dwordx2 v[182:183], v[36:37], off offset:1024
	global_load_dwordx4 v[26:29], v[34:35], off offset:128
	global_load_dwordx4 v[6:9], v207, s[26:27]
	s_nop 0
	global_load_dwordx4 v[10:13], v[10:11], off offset:3072
	s_nop 0
	global_load_dwordx2 v[184:185], v[36:37], off offset:1536
	s_nop 0
	global_load_dwordx4 v[34:37], v[34:35], off offset:192
	s_cbranch_scc1 .LBB0_1325
	s_add_i32 s8, s12, 0
	s_add_i32 s8, s8, 0x10020
	v_mov_b32_e32 v162, s8
	ds_read_b32 v162, v162
	s_waitcnt lgkmcnt(0)
	v_add_u32_e32 v162, 8, v162
	v_cmp_lt_u32_e32 vcc, s11, v162
	s_cbranch_vccnz .LBB0_1325

.LBB0_1325:
	s_lshl_b32 s2, s11, 11
	s_and_b32 s2, s2, 0x3000
	v_add_u32_e32 v162, s2, v177
	v_cvt_pk_bf16_f32 v170, v158, v159
	v_cvt_pk_bf16_f32 v171, v160, v161
	v_cvt_pk_bf16_f32 v172, v94, v95
	v_cvt_pk_bf16_f32 v173, v96, v97
	v_cvt_pk_bf16_f32 v166, v150, v151
	v_cvt_pk_bf16_f32 v167, v152, v153
	v_cvt_pk_bf16_f32 v168, v154, v155
	v_cvt_pk_bf16_f32 v169, v156, v157
	ds_write2st64_b64 v162, v[170:171], v[172:173] offset1:1
	ds_write2st64_b64 v162, v[166:167], v[168:169] offset0:2 offset1:3
	s_nop 1
	v_mov_b32_e32 v222, s12
	v_add_u32_e32 v222, 0x10000, v222
	v_mov_b32_e32 v223, s23
	s_waitcnt vmcnt(45)
	v_lshlrev_b32_e32 v162, 16, v196
	v_and_b32_e32 v163, 0xffff0000, v196
	s_waitcnt vmcnt(44)
	v_pk_fma_f32 v[90:91], v[90:91], v[158:159], v[162:163]
	v_lshlrev_b32_e32 v158, 16, v197
	v_and_b32_e32 v159, 0xffff0000, v197
	v_pk_fma_f32 v[92:93], v[92:93], v[160:161], v[158:159]
	s_sub_i32 s2, 0x78, s18
	s_add_i32 s3, s18, 7
	v_mfma_f32_16x16x32_bf16 v[86:89], v[86:89], v[170:173], v[90:93]
	s_and_b64 s[8:9], s[6:7], exec
	s_cselect_b32 s2, s3, s2
	s_add_i32 s8, s2, s19
	v_mfma_f32_16x16x32_bf16 v[158:161], v[78:81], v[166:169], v[86:89]
	s_waitcnt lgkmcnt(0)
	s_mov_b64 s[98:99], exec
	s_mov_b64 exec, s[0:1]
	ds_write_b32 v222, v223
	s_mov_b64 exec, s[98:99]
	s_waitcnt vmcnt(41)
	v_lshlrev_b32_e32 v78, 16, v194
	v_and_b32_e32 v79, 0xffff0000, v194
	v_lshlrev_b32_e32 v80, 16, v195
	v_and_b32_e32 v81, 0xffff0000, v195
	s_waitcnt vmcnt(40)
	v_pk_fma_f32 v[78:79], v[82:83], v[94:95], v[78:79]
	v_pk_fma_f32 v[80:81], v[84:85], v[96:97], v[80:81]
	s_ashr_i32 s9, s8, 31
	s_lshl_b64 s[24:25], s[8:9], 13
	v_mfma_f32_16x16x32_bf16 v[62:65], v[62:65], v[170:173], v[78:81]
	s_add_u32 s26, s20, s24
	s_addc_u32 s27, s21, s25
	s_lshl_b64 s[8:9], s[8:9], 8
	v_mfma_f32_16x16x32_bf16 v[162:165], v[66:69], v[166:169], v[62:65]
	v_lshl_add_u64 v[90:91], v[178:179], 0, s[8:9]
	v_lshl_add_u64 v[86:87], v[180:181], 0, s[24:25]
	s_cmp_lt_u32 s18, 3
	s_waitcnt vmcnt(37)
	v_lshlrev_b32_e32 v62, 16, v190
	v_and_b32_e32 v63, 0xffff0000, v190
	v_lshlrev_b32_e32 v64, 16, v191
	v_and_b32_e32 v65, 0xffff0000, v191
	s_waitcnt vmcnt(36)
	v_pk_fma_f32 v[62:63], v[70:71], v[150:151], v[62:63]
	v_pk_fma_f32 v[64:65], v[72:73], v[152:153], v[64:65]
	global_load_dwordx4 v[78:81], v174, s[26:27]
	global_load_dwordx4 v[70:73], v174, s[26:27] offset:1024
	v_mfma_f32_16x16x32_bf16 v[50:53], v[50:53], v[170:173], v[62:65]
	v_mfma_f32_16x16x32_bf16 v[150:153], v[58:61], v[166:169], v[50:53]
	s_waitcnt vmcnt(35)
	s_nop 5
	v_lshlrev_b32_e32 v50, 16, v192
	v_and_b32_e32 v51, 0xffff0000, v192
	v_lshlrev_b32_e32 v52, 16, v193
	v_and_b32_e32 v53, 0xffff0000, v193
	s_waitcnt vmcnt(34)
	v_pk_fma_f32 v[50:51], v[74:75], v[154:155], v[50:51]
	v_pk_fma_f32 v[52:53], v[76:77], v[156:157], v[52:53]
	s_nop 1
	v_mfma_f32_16x16x32_bf16 v[154:157], v[54:57], v[170:173], v[50:53]
	v_lshl_add_u64 v[54:55], s[26:27], 0, v[174:175]
	v_add_co_u32_e32 v66, vcc, 0x1000, v54
	s_nop 0
	global_load_dwordx4 v[50:53], v174, s[26:27] offset:2048
	global_load_dwordx4 v[58:61], v174, s[26:27] offset:3072
	global_load_dwordx4 v[94:97], v[90:91], off
	global_load_dwordx4 v[82:85], v[90:91], off offset:64
	v_addc_co_u32_e32 v67, vcc, 0, v55, vcc
	global_load_dwordx4 v[54:57], v206, s[26:27]
	global_load_dwordx4 v[62:65], v207, s[26:27]
	global_load_dwordx4 v[74:77], v[66:67], off offset:1024
	s_nop 0
	global_load_dwordx4 v[66:69], v[66:67], off offset:3072
	s_nop 0
	global_load_dwordx2 v[196:197], v[86:87], off
	global_load_dwordx2 v[194:195], v[86:87], off offset:512
	global_load_dwordx2 v[190:191], v[86:87], off offset:1024
	global_load_dwordx2 v[192:193], v[86:87], off offset:1536
	s_nop 0
	global_load_dwordx4 v[86:89], v[90:91], off offset:128
	s_nop 0
	global_load_dwordx4 v[90:93], v[90:91], off offset:192
	v_mfma_f32_16x16x32_bf16 v[106:109], v[106:109], v[166:169], v[154:157]
	s_cbranch_scc1 .LBB0_1330
	s_add_i32 s8, s12, 0
	s_add_i32 s8, s8, 0x10020
	v_mov_b32_e32 v154, s8
	ds_read_b32 v154, v154
	s_waitcnt lgkmcnt(0)
	v_add_u32_e32 v154, 8, v154
	v_cmp_lt_u32_e32 vcc, s23, v154
	s_cbranch_vccnz .LBB0_1330

.LBB0_1330:
	s_lshl_b32 s2, s23, 11
	s_and_b32 s2, s2, 0x3800
	v_add_u32_e32 v154, s2, v177
	v_cvt_pk_bf16_f32 v170, v158, v159
	v_cvt_pk_bf16_f32 v171, v160, v161
	v_cvt_pk_bf16_f32 v172, v162, v163
	v_cvt_pk_bf16_f32 v173, v164, v165
	v_cvt_pk_bf16_f32 v166, v150, v151
	v_cvt_pk_bf16_f32 v167, v152, v153
	v_cvt_pk_bf16_f32 v168, v106, v107
	v_cvt_pk_bf16_f32 v169, v108, v109
	ds_write2st64_b64 v154, v[170:171], v[172:173] offset1:1
	ds_write2st64_b64 v154, v[166:167], v[168:169] offset0:2 offset1:3
	s_nop 1
	v_mov_b32_e32 v222, s12
	v_add_u32_e32 v222, 0x10000, v222
	v_mov_b32_e32 v223, s10
	s_waitcnt vmcnt(45)
	v_lshlrev_b32_e32 v154, 16, v204
	v_and_b32_e32 v155, 0xffff0000, v204
	s_waitcnt vmcnt(44)
	v_pk_fma_f32 v[146:147], v[146:147], v[158:159], v[154:155]
	v_lshlrev_b32_e32 v154, 16, v205
	v_and_b32_e32 v155, 0xffff0000, v205
	v_pk_fma_f32 v[148:149], v[148:149], v[160:161], v[154:155]
	s_cmpk_lt_u32 s18, 0x78
	s_nop 0
	v_mfma_f32_16x16x32_bf16 v[142:145], v[142:145], v[170:173], v[146:149]
	v_mfma_f32_16x16x32_bf16 v[158:161], v[134:137], v[166:169], v[142:145]
	s_waitcnt lgkmcnt(0)
	s_mov_b64 s[98:99], exec
	s_mov_b64 exec, s[0:1]
	ds_write_b32 v222, v223
	s_mov_b64 exec, s[98:99]
	s_waitcnt vmcnt(41)
	v_lshlrev_b32_e32 v134, 16, v202
	v_and_b32_e32 v135, 0xffff0000, v202
	v_lshlrev_b32_e32 v136, 16, v203
	v_and_b32_e32 v137, 0xffff0000, v203
	s_waitcnt vmcnt(40)
	v_pk_fma_f32 v[134:135], v[138:139], v[162:163], v[134:135]
	v_pk_fma_f32 v[136:137], v[140:141], v[164:165], v[136:137]
	s_nop 1
	v_mfma_f32_16x16x32_bf16 v[118:121], v[118:121], v[170:173], v[134:137]
	v_mfma_f32_16x16x32_bf16 v[154:157], v[122:125], v[166:169], v[118:121]
	s_waitcnt vmcnt(37)
	s_nop 5
	v_lshlrev_b32_e32 v118, 16, v198
	v_and_b32_e32 v119, 0xffff0000, v198
	v_lshlrev_b32_e32 v120, 16, v199
	v_and_b32_e32 v121, 0xffff0000, v199
	s_waitcnt vmcnt(36)
	v_pk_fma_f32 v[118:119], v[126:127], v[150:151], v[118:119]
	v_pk_fma_f32 v[120:121], v[128:129], v[152:153], v[120:121]
	s_nop 1
	v_mfma_f32_16x16x32_bf16 v[102:105], v[102:105], v[170:173], v[118:121]
	v_mfma_f32_16x16x32_bf16 v[150:153], v[114:117], v[166:169], v[102:105]
	s_waitcnt vmcnt(33)
	s_nop 5
	v_lshlrev_b32_e32 v102, 16, v200
	v_and_b32_e32 v103, 0xffff0000, v200
	v_lshlrev_b32_e32 v104, 16, v201
	v_and_b32_e32 v105, 0xffff0000, v201
	s_waitcnt vmcnt(32)
	v_pk_fma_f32 v[102:103], v[130:131], v[106:107], v[102:103]
	v_pk_fma_f32 v[104:105], v[132:133], v[108:109], v[104:105]
	s_nop 1
	v_mfma_f32_16x16x32_bf16 v[102:105], v[110:113], v[170:173], v[102:105]
	v_mfma_f32_16x16x32_bf16 v[106:109], v[98:101], v[166:169], v[102:105]
	s_cbranch_scc0 .LBB0_1334
	s_mov_b32 s18, s10
	s_branch .LBB0_1302

.LBB0_3623:
	s_lshl_b32 s2, s20, 11
	s_and_b32 s2, s2, 0x3000
	v_add_u32_e32 v162, s2, v189
	v_cvt_pk_bf16_f32 v174, v154, v155
	v_cvt_pk_bf16_f32 v175, v156, v157
	v_cvt_pk_bf16_f32 v176, v150, v151
	v_cvt_pk_bf16_f32 v177, v152, v153
	v_cvt_pk_bf16_f32 v178, v102, v103
	v_cvt_pk_bf16_f32 v179, v104, v105
	v_cvt_pk_bf16_f32 v180, v106, v107
	v_cvt_pk_bf16_f32 v181, v108, v109
	ds_write2st64_b64 v162, v[174:175], v[176:177] offset1:1
	ds_write2st64_b64 v162, v[178:179], v[180:181] offset0:2 offset1:3
	s_nop 1
	s_or_b32 s17, s20, 1
	v_mov_b32_e32 v222, s9
	v_add_u32_e32 v222, 0x10000, v222
	v_mov_b32_e32 v223, s17
	s_waitcnt vmcnt(37)
	v_lshlrev_b32_e32 v162, 16, v196
	v_and_b32_e32 v163, 0xffff0000, v196
	v_pk_fma_f32 v[46:47], v[154:155], v[46:47], v[162:163]
	v_lshlrev_b32_e32 v154, 16, v197
	v_and_b32_e32 v155, 0xffff0000, v197
	v_pk_fma_f32 v[48:49], v[156:157], v[48:49], v[154:155]
	s_sub_i32 s15, 0x7c, s20
	s_add_i32 s14, s20, 3
	v_mfma_f32_16x16x32_bf16 v[42:45], v[42:45], v[174:177], v[46:49]
	s_and_b64 s[2:3], s[6:7], exec
	s_cselect_b32 s2, s14, s15
	s_add_i32 s2, s2, s21
	v_mfma_f32_16x16x32_bf16 v[170:173], v[34:37], v[178:181], v[42:45]
	s_waitcnt lgkmcnt(0)
	s_mov_b64 s[98:99], exec
	s_mov_b64 exec, s[0:1]
	ds_write_b32 v222, v223
	s_mov_b64 exec, s[98:99]
	s_waitcnt vmcnt(36)
	v_lshlrev_b32_e32 v34, 16, v184
	v_and_b32_e32 v35, 0xffff0000, v184
	v_pk_fma_f32 v[26:27], v[150:151], v[26:27], v[34:35]
	v_lshlrev_b32_e32 v34, 16, v185
	v_and_b32_e32 v35, 0xffff0000, v185
	v_pk_fma_f32 v[28:29], v[152:153], v[28:29], v[34:35]
	s_ashr_i32 s3, s2, 31
	s_lshl_b64 s[26:27], s[2:3], 13
	v_mfma_f32_16x16x32_bf16 v[18:21], v[18:21], v[174:177], v[26:29]
	s_add_u32 s28, s22, s26
	s_addc_u32 s29, s23, s27
	s_lshl_b64 s[2:3], s[2:3], 8
	v_mfma_f32_16x16x32_bf16 v[166:169], v[22:25], v[178:181], v[18:21]
	v_lshl_add_u64 v[22:23], v[190:191], 0, s[2:3]
	v_lshl_add_u64 v[24:25], v[192:193], 0, s[26:27]
	global_load_dwordx4 v[154:157], v186, s[28:29]
	global_load_dwordx4 v[150:153], v186, s[28:29] offset:1024
	s_waitcnt vmcnt(37)
	v_lshlrev_b32_e32 v18, 16, v182
	v_and_b32_e32 v19, 0xffff0000, v182
	v_lshlrev_b32_e32 v20, 16, v183
	v_and_b32_e32 v21, 0xffff0000, v183
	s_waitcnt vmcnt(35)
	v_pk_fma_f32 v[18:19], v[102:103], v[30:31], v[18:19]
	v_pk_fma_f32 v[20:21], v[104:105], v[32:33], v[20:21]
	s_waitcnt vmcnt(29)
	s_nop 0
	v_mfma_f32_16x16x32_bf16 v[182:185], v[38:41], v[174:177], v[18:21]
	global_load_dwordx4 v[34:37], v186, s[28:29] offset:2048
	global_load_dwordx4 v[38:41], v186, s[28:29] offset:3072
	global_load_dwordx4 v[162:165], v[22:23], off
	global_load_dwordx4 v[46:49], v[22:23], off offset:64
	v_lshl_add_u64 v[18:19], s[28:29], 0, v[186:187]
	v_add_co_u32_e32 v42, vcc, 0x1000, v18
	v_mfma_f32_16x16x32_bf16 v[182:185], v[10:13], v[178:181], v[182:185]
	s_nop 0
	v_addc_co_u32_e32 v43, vcc, 0, v19, vcc
	global_load_dwordx4 v[26:29], v220, s[28:29]
	global_load_dwordx4 v[18:21], v221, s[28:29]
	global_load_dwordx4 v[30:33], v[42:43], off offset:1024
	global_load_dwordx4 v[102:105], v[42:43], off offset:3072
	global_load_dwordx2 v[218:219], v[24:25], off
	global_load_dwordx2 v[214:215], v[24:25], off offset:512
	global_load_dwordx2 v[210:211], v[24:25], off offset:1024
	global_load_dwordx2 v[196:197], v[24:25], off offset:1536
	s_nop 0
	global_load_dwordx4 v[42:45], v[22:23], off offset:128
	s_nop 0
	global_load_dwordx4 v[22:25], v[22:23], off offset:192
	v_lshlrev_b32_e32 v10, 16, v194
	v_and_b32_e32 v11, 0xffff0000, v194
	v_pk_fma_f32 v[6:7], v[106:107], v[6:7], v[10:11]
	v_lshlrev_b32_e32 v10, 16, v195
	v_and_b32_e32 v11, 0xffff0000, v195
	v_pk_fma_f32 v[8:9], v[108:109], v[8:9], v[10:11]
	s_andn2_b64 vcc, exec, s[12:13]
	s_waitcnt vmcnt(41)
	v_mfma_f32_16x16x32_bf16 v[6:9], v[14:17], v[174:177], v[6:9]
	v_mfma_f32_16x16x32_bf16 v[106:109], v[2:5], v[178:181], v[6:9]
	s_cbranch_vccnz .LBB0_3628
	s_add_i32 s12, s9, 0
	s_add_i32 s12, s12, 0x10020
	v_mov_b32_e32 v2, s12
	ds_read_b32 v2, v2
	s_waitcnt lgkmcnt(0)
	v_add_u32_e32 v2, 8, v2
	v_cmp_lt_u32_e32 vcc, s17, v2
	s_cbranch_vccnz .LBB0_3628

.LBB0_3628:
	s_lshl_b32 s2, s17, 11
	s_and_b32 s2, s2, 0x3800
	v_add_u32_e32 v2, s2, v189
	v_cvt_pk_bf16_f32 v174, v170, v171
	v_cvt_pk_bf16_f32 v175, v172, v173
	v_cvt_pk_bf16_f32 v176, v166, v167
	v_cvt_pk_bf16_f32 v177, v168, v169
	v_cvt_pk_bf16_f32 v14, v182, v183
	v_cvt_pk_bf16_f32 v15, v184, v185
	v_cvt_pk_bf16_f32 v16, v106, v107
	v_cvt_pk_bf16_f32 v17, v108, v109
	ds_write2st64_b64 v2, v[174:175], v[176:177] offset1:1
	ds_write2st64_b64 v2, v[14:15], v[16:17] offset0:2 offset1:3
	s_nop 1
	v_mov_b32_e32 v222, s9
	v_add_u32_e32 v222, 0x10000, v222
	v_mov_b32_e32 v223, s16
	s_waitcnt vmcnt(37)
	v_lshlrev_b32_e32 v2, 16, v204
	v_and_b32_e32 v3, 0xffff0000, v204
	v_lshlrev_b32_e32 v4, 16, v205
	v_and_b32_e32 v5, 0xffff0000, v205
	v_pk_fma_f32 v[2:3], v[94:95], v[170:171], v[2:3]
	v_pk_fma_f32 v[4:5], v[96:97], v[172:173], v[4:5]
	s_sub_i32 s12, 0x7b, s20
	s_add_i32 s15, s20, 4
	v_mfma_f32_16x16x32_bf16 v[2:5], v[86:89], v[174:177], v[2:5]
	s_and_b64 s[2:3], s[6:7], exec
	s_cselect_b32 s2, s15, s12
	s_add_i32 s2, s2, s21
	s_waitcnt vmcnt(35)
	v_lshlrev_b32_e32 v6, 16, v200
	v_and_b32_e32 v7, 0xffff0000, v200
	v_lshlrev_b32_e32 v8, 16, v201
	v_and_b32_e32 v9, 0xffff0000, v201
	s_ashr_i32 s3, s2, 31
	v_mfma_f32_16x16x32_bf16 v[10:13], v[78:81], v[14:17], v[2:5]
	s_waitcnt lgkmcnt(0)
	s_mov_b64 s[98:99], exec
	s_mov_b64 exec, s[0:1]
	ds_write_b32 v222, v223
	s_mov_b64 exec, s[98:99]
	s_waitcnt vmcnt(33)
	v_pk_fma_f32 v[6:7], v[90:91], v[182:183], v[6:7]
	v_pk_fma_f32 v[8:9], v[92:93], v[184:185], v[8:9]
	s_lshl_b64 s[12:13], s[2:3], 13
	v_lshlrev_b32_e32 v2, 16, v202
	v_and_b32_e32 v3, 0xffff0000, v202
	v_lshlrev_b32_e32 v4, 16, v203
	v_and_b32_e32 v5, 0xffff0000, v203
	v_pk_fma_f32 v[2:3], v[82:83], v[166:167], v[2:3]
	v_pk_fma_f32 v[4:5], v[84:85], v[168:169], v[4:5]
	v_mfma_f32_16x16x32_bf16 v[6:9], v[58:61], v[174:177], v[6:9]
	v_lshlrev_b32_e32 v58, 16, v198
	v_and_b32_e32 v59, 0xffff0000, v198
	v_lshlrev_b32_e32 v60, 16, v199
	v_and_b32_e32 v61, 0xffff0000, v199
	s_add_u32 s26, s22, s12
	v_mfma_f32_16x16x32_bf16 v[2:5], v[62:65], v[174:177], v[2:5]
	s_waitcnt vmcnt(32)
	v_pk_fma_f32 v[58:59], v[74:75], v[106:107], v[58:59]
	v_pk_fma_f32 v[60:61], v[76:77], v[108:109], v[60:61]
	s_addc_u32 s27, s23, s13
	s_lshl_b64 s[2:3], s[2:3], 8
	v_mfma_f32_16x16x32_bf16 v[166:169], v[54:57], v[174:177], v[58:61]
	v_lshl_add_u64 v[54:55], s[26:27], 0, v[186:187]
	v_add_co_u32_e32 v78, vcc, 0x1000, v54
	s_nop 0
	v_lshl_add_u64 v[58:59], v[190:191], 0, s[2:3]
	v_lshl_add_u64 v[60:61], v[192:193], 0, s[12:13]
	v_addc_co_u32_e32 v79, vcc, 0, v55, vcc
	v_mfma_f32_16x16x32_bf16 v[2:5], v[66:69], v[14:17], v[2:5]
	global_load_dwordx4 v[90:93], v186, s[26:27]
	global_load_dwordx4 v[86:89], v186, s[26:27] offset:1024
	s_cmp_lt_u32 s20, 6
	v_mfma_f32_16x16x32_bf16 v[6:9], v[70:73], v[14:17], v[6:9]
	global_load_dwordx4 v[70:73], v186, s[26:27] offset:2048
	global_load_dwordx4 v[74:77], v186, s[26:27] offset:3072
	global_load_dwordx4 v[94:97], v[58:59], off
	global_load_dwordx4 v[82:85], v[58:59], off offset:64
	global_load_dwordx4 v[62:65], v220, s[26:27]
	global_load_dwordx4 v[54:57], v221, s[26:27]
	global_load_dwordx4 v[66:69], v[78:79], off offset:1024
	global_load_dwordx4 v[106:109], v[78:79], off offset:3072
	global_load_dwordx2 v[202:203], v[60:61], off
	global_load_dwordx2 v[200:201], v[60:61], off offset:512
	global_load_dwordx2 v[198:199], v[60:61], off offset:1024
	global_load_dwordx2 v[178:179], v[60:61], off offset:1536
	s_nop 0
	global_load_dwordx4 v[78:81], v[58:59], off offset:128
	s_nop 0
	global_load_dwordx4 v[58:61], v[58:59], off offset:192
	v_mfma_f32_16x16x32_bf16 v[50:53], v[50:53], v[14:17], v[166:169]
	s_cbranch_scc1 .LBB0_3633
	s_add_i32 s12, s9, 0
	s_add_i32 s12, s12, 0x10020
	v_mov_b32_e32 v14, s12
	ds_read_b32 v14, v14
	s_waitcnt lgkmcnt(0)
	v_add_u32_e32 v14, 8, v14
	v_cmp_lt_u32_e32 vcc, s16, v14
	s_cbranch_vccnz .LBB0_3633

.LBB0_3633:
	s_lshl_b32 s2, s16, 11
	s_and_b32 s2, s2, 0x3000
	v_add_u32_e32 v170, s2, v189
	v_cvt_pk_bf16_f32 v166, v10, v11
	v_cvt_pk_bf16_f32 v167, v12, v13
	v_cvt_pk_bf16_f32 v168, v2, v3
	v_cvt_pk_bf16_f32 v169, v4, v5
	v_cvt_pk_bf16_f32 v14, v6, v7
	v_cvt_pk_bf16_f32 v15, v8, v9
	v_cvt_pk_bf16_f32 v16, v50, v51
	v_cvt_pk_bf16_f32 v17, v52, v53
	ds_write2st64_b64 v170, v[166:167], v[168:169] offset1:1
	ds_write2st64_b64 v170, v[14:15], v[16:17] offset0:2 offset1:3
	s_nop 1
	v_mov_b32_e32 v222, s9
	v_add_u32_e32 v222, 0x10000, v222
	v_mov_b32_e32 v223, s14
	s_waitcnt vmcnt(37)
	v_lshlrev_b32_e32 v170, 16, v216
	v_and_b32_e32 v171, 0xffff0000, v216
	v_pk_fma_f32 v[10:11], v[158:159], v[10:11], v[170:171]
	v_lshlrev_b32_e32 v158, 16, v217
	v_and_b32_e32 v159, 0xffff0000, v217
	v_pk_fma_f32 v[12:13], v[160:161], v[12:13], v[158:159]
	s_sub_i32 s12, 0x7a, s20
	s_add_i32 s16, s20, 5
	v_mfma_f32_16x16x32_bf16 v[10:13], v[146:149], v[166:169], v[10:13]
	s_and_b64 s[2:3], s[6:7], exec
	s_cselect_b32 s2, s16, s12
	s_add_i32 s2, s2, s21
	v_mfma_f32_16x16x32_bf16 v[10:13], v[142:145], v[14:17], v[10:13]
	s_waitcnt lgkmcnt(0)
	s_mov_b64 s[98:99], exec
	s_mov_b64 exec, s[0:1]
	ds_write_b32 v222, v223
	s_mov_b64 exec, s[98:99]
	s_waitcnt vmcnt(36)
	v_lshlrev_b32_e32 v142, 16, v212
	v_and_b32_e32 v143, 0xffff0000, v212
	v_pk_fma_f32 v[2:3], v[138:139], v[2:3], v[142:143]
	v_lshlrev_b32_e32 v138, 16, v213
	v_and_b32_e32 v139, 0xffff0000, v213
	v_pk_fma_f32 v[4:5], v[140:141], v[4:5], v[138:139]
	s_ashr_i32 s3, s2, 31
	s_lshl_b64 s[12:13], s[2:3], 13
	v_mfma_f32_16x16x32_bf16 v[2:5], v[126:129], v[166:169], v[2:5]
	s_waitcnt vmcnt(35)
	v_lshlrev_b32_e32 v126, 16, v208
	v_and_b32_e32 v127, 0xffff0000, v208
	s_waitcnt vmcnt(33)
	v_pk_fma_f32 v[6:7], v[134:135], v[6:7], v[126:127]
	v_lshlrev_b32_e32 v126, 16, v209
	v_and_b32_e32 v127, 0xffff0000, v209
	v_pk_fma_f32 v[8:9], v[136:137], v[8:9], v[126:127]
	s_add_u32 s26, s22, s12
	s_addc_u32 s27, s23, s13
	v_mfma_f32_16x16x32_bf16 v[6:9], v[118:121], v[166:169], v[6:9]
	v_lshlrev_b32_e32 v118, 16, v206
	v_and_b32_e32 v119, 0xffff0000, v206
	s_waitcnt vmcnt(32)
	v_pk_fma_f32 v[50:51], v[114:115], v[50:51], v[118:119]
	v_lshlrev_b32_e32 v114, 16, v207
	v_and_b32_e32 v115, 0xffff0000, v207
	v_pk_fma_f32 v[52:53], v[116:117], v[52:53], v[114:115]
	s_lshl_b64 s[2:3], s[2:3], 8
	v_lshl_add_u64 v[118:119], v[190:191], 0, s[2:3]
	v_mfma_f32_16x16x32_bf16 v[50:53], v[110:113], v[166:169], v[50:53]
	v_lshl_add_u64 v[110:111], s[26:27], 0, v[186:187]
	v_add_co_u32_e32 v110, vcc, 0x1000, v110
	v_lshl_add_u64 v[120:121], v[192:193], 0, s[12:13]
	s_nop 0
	v_addc_co_u32_e32 v111, vcc, 0, v111, vcc
	v_mfma_f32_16x16x32_bf16 v[2:5], v[130:133], v[14:17], v[2:5]
	global_load_dwordx4 v[158:161], v186, s[26:27]
	global_load_dwordx4 v[146:149], v186, s[26:27] offset:1024
	global_load_dwordx4 v[130:133], v186, s[26:27] offset:2048
	global_load_dwordx4 v[134:137], v186, s[26:27] offset:3072
	global_load_dwordx4 v[166:169], v[118:119], off
	global_load_dwordx4 v[142:145], v[118:119], off offset:64
	s_cmp_lt_u32 s20, 5
	v_mfma_f32_16x16x32_bf16 v[6:9], v[122:125], v[14:17], v[6:9]
	global_load_dwordx4 v[122:125], v220, s[26:27]
	global_load_dwordx4 v[114:117], v221, s[26:27]
	global_load_dwordx4 v[126:129], v[110:111], off offset:1024
	s_nop 0
	global_load_dwordx4 v[110:113], v[110:111], off offset:3072
	s_nop 0
	global_load_dwordx2 v[212:213], v[120:121], off
	global_load_dwordx2 v[208:209], v[120:121], off offset:512
	global_load_dwordx2 v[206:207], v[120:121], off offset:1024
	global_load_dwordx2 v[180:181], v[120:121], off offset:1536
	global_load_dwordx4 v[138:141], v[118:119], off offset:128
	s_nop 0
	global_load_dwordx4 v[118:121], v[118:119], off offset:192
	v_mfma_f32_16x16x32_bf16 v[14:17], v[98:101], v[14:17], v[50:53]
	s_cbranch_scc1 .LBB0_3638
	s_add_i32 s12, s9, 0
	s_add_i32 s12, s12, 0x10020
	v_mov_b32_e32 v50, s12
	ds_read_b32 v50, v50
	s_waitcnt lgkmcnt(0)
	v_add_u32_e32 v50, 8, v50
	v_cmp_lt_u32_e32 vcc, s14, v50
	s_cbranch_vccnz .LBB0_3638

.LBB0_3638:
	s_lshl_b32 s2, s14, 11
	s_and_b32 s2, s2, 0x3800
	v_add_u32_e32 v50, s2, v189
	v_cvt_pk_bf16_f32 v174, v10, v11
	v_cvt_pk_bf16_f32 v175, v12, v13
	v_cvt_pk_bf16_f32 v176, v2, v3
	v_cvt_pk_bf16_f32 v177, v4, v5
	v_cvt_pk_bf16_f32 v170, v6, v7
	v_cvt_pk_bf16_f32 v171, v8, v9
	v_cvt_pk_bf16_f32 v172, v14, v15
	v_cvt_pk_bf16_f32 v173, v16, v17
	ds_write2st64_b64 v50, v[174:175], v[176:177] offset1:1
	ds_write2st64_b64 v50, v[170:171], v[172:173] offset0:2 offset1:3
	s_nop 1
	v_mov_b32_e32 v222, s9
	v_add_u32_e32 v222, 0x10000, v222
	v_mov_b32_e32 v223, s15
	s_waitcnt vmcnt(37)
	v_lshlrev_b32_e32 v50, 16, v218
	v_and_b32_e32 v51, 0xffff0000, v218
	v_pk_fma_f32 v[10:11], v[162:163], v[10:11], v[50:51]
	v_lshlrev_b32_e32 v50, 16, v219
	v_and_b32_e32 v51, 0xffff0000, v219
	v_pk_fma_f32 v[12:13], v[164:165], v[12:13], v[50:51]
	s_sub_i32 s12, 0x79, s20
	s_add_i32 s14, s20, 6
	v_mfma_f32_16x16x32_bf16 v[10:13], v[154:157], v[174:177], v[10:13]
	s_and_b64 s[2:3], s[6:7], exec
	s_cselect_b32 s2, s14, s12
	s_add_i32 s2, s2, s21
	v_mfma_f32_16x16x32_bf16 v[150:153], v[150:153], v[170:173], v[10:13]
	s_waitcnt lgkmcnt(0)
	s_mov_b64 s[98:99], exec
	s_mov_b64 exec, s[0:1]
	ds_write_b32 v222, v223
	s_mov_b64 exec, s[98:99]
	s_ashr_i32 s3, s2, 31
	s_lshl_b64 s[12:13], s[2:3], 13
	s_add_u32 s26, s22, s12
	s_waitcnt vmcnt(36)
	v_lshlrev_b32_e32 v10, 16, v214
	v_and_b32_e32 v11, 0xffff0000, v214
	v_pk_fma_f32 v[2:3], v[46:47], v[2:3], v[10:11]
	v_lshlrev_b32_e32 v10, 16, v215
	v_and_b32_e32 v11, 0xffff0000, v215
	v_pk_fma_f32 v[4:5], v[48:49], v[4:5], v[10:11]
	s_addc_u32 s27, s23, s13
	s_lshl_b64 s[2:3], s[2:3], 8
	v_mfma_f32_16x16x32_bf16 v[2:5], v[34:37], v[174:177], v[2:5]
	s_cmp_lt_u32 s20, 4
	v_mfma_f32_16x16x32_bf16 v[50:53], v[38:41], v[170:173], v[2:5]
	s_waitcnt vmcnt(35)
	s_nop 4
	v_lshlrev_b32_e32 v2, 16, v210
	v_and_b32_e32 v3, 0xffff0000, v210
	v_lshlrev_b32_e32 v4, 16, v211
	v_and_b32_e32 v5, 0xffff0000, v211
	s_waitcnt vmcnt(33)
	v_pk_fma_f32 v[2:3], v[42:43], v[6:7], v[2:3]
	v_pk_fma_f32 v[4:5], v[44:45], v[8:9], v[4:5]
	v_lshl_add_u64 v[6:7], v[190:191], 0, s[2:3]
	v_lshl_add_u64 v[8:9], v[192:193], 0, s[12:13]
	v_mfma_f32_16x16x32_bf16 v[2:5], v[26:29], v[174:177], v[2:5]
	global_load_dwordx4 v[42:45], v186, s[26:27]
	global_load_dwordx4 v[34:37], v186, s[26:27] offset:1024
	v_mfma_f32_16x16x32_bf16 v[98:101], v[30:33], v[170:173], v[2:5]
	s_nop 4
	v_lshlrev_b32_e32 v2, 16, v196
	v_and_b32_e32 v3, 0xffff0000, v196
	v_lshlrev_b32_e32 v4, 16, v197
	v_and_b32_e32 v5, 0xffff0000, v197
	s_waitcnt vmcnt(34)
	v_pk_fma_f32 v[2:3], v[22:23], v[14:15], v[2:3]
	v_pk_fma_f32 v[4:5], v[24:25], v[16:17], v[4:5]
	s_nop 1
	v_mfma_f32_16x16x32_bf16 v[154:157], v[18:21], v[174:177], v[2:5]
	global_load_dwordx4 v[18:21], v186, s[26:27] offset:2048
	global_load_dwordx4 v[22:25], v186, s[26:27] offset:3072
	global_load_dwordx4 v[46:49], v[6:7], off
	global_load_dwordx4 v[26:29], v[6:7], off offset:64
	v_lshl_add_u64 v[2:3], s[26:27], 0, v[186:187]
	v_add_co_u32_e32 v2, vcc, 0x1000, v2
	v_mfma_f32_16x16x32_bf16 v[162:165], v[102:105], v[170:173], v[154:157]
	s_nop 0
	v_addc_co_u32_e32 v3, vcc, 0, v3, vcc
	global_load_dwordx4 v[38:41], v220, s[26:27]
	global_load_dwordx4 v[14:17], v221, s[26:27]
	global_load_dwordx4 v[10:13], v[2:3], off offset:1024
	s_nop 0
	global_load_dwordx4 v[2:5], v[2:3], off offset:3072
	s_nop 0
	global_load_dwordx2 v[196:197], v[8:9], off
	global_load_dwordx2 v[184:185], v[8:9], off offset:512
	global_load_dwordx2 v[182:183], v[8:9], off offset:1024
	global_load_dwordx2 v[194:195], v[8:9], off offset:1536
	global_load_dwordx4 v[30:33], v[6:7], off offset:128
	s_nop 0
	global_load_dwordx4 v[6:9], v[6:7], off offset:192
	s_cbranch_scc1 .LBB0_3643
	s_add_i32 s12, s9, 0
	s_add_i32 s12, s12, 0x10020
	v_mov_b32_e32 v102, s12
	ds_read_b32 v102, v102
	s_waitcnt lgkmcnt(0)
	v_add_u32_e32 v102, 8, v102
	v_cmp_lt_u32_e32 vcc, s15, v102
	s_cbranch_vccnz .LBB0_3643

.LBB0_3643:
	s_lshl_b32 s2, s15, 11
	s_and_b32 s2, s2, 0x3000
	v_add_u32_e32 v102, s2, v189
	v_cvt_pk_bf16_f32 v170, v150, v151
	v_cvt_pk_bf16_f32 v171, v152, v153
	v_cvt_pk_bf16_f32 v172, v50, v51
	v_cvt_pk_bf16_f32 v173, v52, v53
	v_cvt_pk_bf16_f32 v154, v98, v99
	v_cvt_pk_bf16_f32 v155, v100, v101
	v_cvt_pk_bf16_f32 v156, v162, v163
	v_cvt_pk_bf16_f32 v157, v164, v165
	ds_write2st64_b64 v102, v[170:171], v[172:173] offset1:1
	ds_write2st64_b64 v102, v[154:155], v[156:157] offset0:2 offset1:3
	s_nop 1
	v_mov_b32_e32 v222, s9
	v_add_u32_e32 v222, 0x10000, v222
	v_mov_b32_e32 v223, s16
	s_waitcnt vmcnt(37)
	v_lshlrev_b32_e32 v102, 16, v202
	v_and_b32_e32 v103, 0xffff0000, v202
	v_pk_fma_f32 v[94:95], v[94:95], v[150:151], v[102:103]
	v_lshlrev_b32_e32 v102, 16, v203
	v_and_b32_e32 v103, 0xffff0000, v203
	v_pk_fma_f32 v[96:97], v[96:97], v[152:153], v[102:103]
	s_sub_i32 s12, 0x78, s20
	s_add_i32 s13, s20, 7
	v_mfma_f32_16x16x32_bf16 v[90:93], v[90:93], v[170:173], v[94:97]
	s_and_b64 s[2:3], s[6:7], exec
	s_cselect_b32 s2, s13, s12
	s_add_i32 s2, s2, s21
	v_mfma_f32_16x16x32_bf16 v[150:153], v[86:89], v[154:157], v[90:93]
	s_waitcnt lgkmcnt(0)
	s_mov_b64 s[98:99], exec
	s_mov_b64 exec, s[0:1]
	ds_write_b32 v222, v223
	s_mov_b64 exec, s[98:99]
	s_waitcnt vmcnt(36)
	v_lshlrev_b32_e32 v86, 16, v200
	v_and_b32_e32 v87, 0xffff0000, v200
	v_pk_fma_f32 v[50:51], v[82:83], v[50:51], v[86:87]
	v_lshlrev_b32_e32 v82, 16, v201
	v_and_b32_e32 v83, 0xffff0000, v201
	v_pk_fma_f32 v[52:53], v[84:85], v[52:53], v[82:83]
	s_ashr_i32 s3, s2, 31
	s_lshl_b64 s[12:13], s[2:3], 13
	v_mfma_f32_16x16x32_bf16 v[50:53], v[70:73], v[170:173], v[50:53]
	s_add_u32 s26, s22, s12
	s_addc_u32 s27, s23, s13
	s_lshl_b64 s[2:3], s[2:3], 8
	v_mfma_f32_16x16x32_bf16 v[102:105], v[74:77], v[154:157], v[50:53]
	v_lshl_add_u64 v[74:75], v[190:191], 0, s[2:3]
	v_lshl_add_u64 v[76:77], v[192:193], 0, s[12:13]
	s_cmp_lt_u32 s20, 3
	s_waitcnt vmcnt(35)
	v_lshlrev_b32_e32 v50, 16, v198
	v_and_b32_e32 v51, 0xffff0000, v198
	v_lshlrev_b32_e32 v52, 16, v199
	v_and_b32_e32 v53, 0xffff0000, v199
	s_waitcnt vmcnt(33)
	v_pk_fma_f32 v[50:51], v[78:79], v[98:99], v[50:51]
	v_pk_fma_f32 v[52:53], v[80:81], v[100:101], v[52:53]
	global_load_dwordx4 v[86:89], v186, s[26:27]
	global_load_dwordx4 v[78:81], v186, s[26:27] offset:1024
	v_mfma_f32_16x16x32_bf16 v[50:53], v[62:65], v[170:173], v[50:53]
	v_mfma_f32_16x16x32_bf16 v[98:101], v[66:69], v[154:157], v[50:53]
	global_load_dwordx4 v[62:65], v186, s[26:27] offset:2048
	global_load_dwordx4 v[66:69], v186, s[26:27] offset:3072
	global_load_dwordx4 v[94:97], v[74:75], off
	global_load_dwordx4 v[82:85], v[74:75], off offset:64
	s_nop 2
	v_lshlrev_b32_e32 v50, 16, v178
	v_and_b32_e32 v51, 0xffff0000, v178
	v_lshlrev_b32_e32 v52, 16, v179
	v_and_b32_e32 v53, 0xffff0000, v179
	s_waitcnt vmcnt(38)
	v_pk_fma_f32 v[50:51], v[58:59], v[162:163], v[50:51]
	v_pk_fma_f32 v[52:53], v[60:61], v[164:165], v[52:53]
	s_nop 1
	v_mfma_f32_16x16x32_bf16 v[162:165], v[54:57], v[170:173], v[50:53]
	s_nop 2
	v_lshl_add_u64 v[50:51], s[26:27], 0, v[186:187]
	v_add_co_u32_e32 v50, vcc, 0x1000, v50
	v_mfma_f32_16x16x32_bf16 v[106:109], v[106:109], v[154:157], v[162:165]
	s_nop 0
	v_addc_co_u32_e32 v51, vcc, 0, v51, vcc
	global_load_dwordx4 v[58:61], v220, s[26:27]
	global_load_dwordx4 v[54:57], v221, s[26:27]
	global_load_dwordx4 v[70:73], v[50:51], off offset:1024
	s_nop 0
	global_load_dwordx4 v[50:53], v[50:51], off offset:3072
	s_nop 0
	global_load_dwordx2 v[204:205], v[76:77], off
	global_load_dwordx2 v[202:203], v[76:77], off offset:512
	global_load_dwordx2 v[200:201], v[76:77], off offset:1024
	global_load_dwordx2 v[198:199], v[76:77], off offset:1536
	global_load_dwordx4 v[90:93], v[74:75], off offset:128
	s_nop 0
	global_load_dwordx4 v[74:77], v[74:75], off offset:192
	s_cbranch_scc1 .LBB0_3648
	s_add_i32 s12, s9, 0
	s_add_i32 s12, s12, 0x10020
	v_mov_b32_e32 v154, s12
	ds_read_b32 v154, v154
	s_waitcnt lgkmcnt(0)
	v_add_u32_e32 v154, 8, v154
	v_cmp_lt_u32_e32 vcc, s16, v154
	s_cbranch_vccnz .LBB0_3648

.LBB0_3648:
	s_lshl_b32 s2, s16, 11
	s_and_b32 s2, s2, 0x3800
	v_add_u32_e32 v154, s2, v189
	v_cvt_pk_bf16_f32 v170, v150, v151
	v_cvt_pk_bf16_f32 v171, v152, v153
	v_cvt_pk_bf16_f32 v172, v102, v103
	v_cvt_pk_bf16_f32 v173, v104, v105
	v_cvt_pk_bf16_f32 v162, v98, v99
	v_cvt_pk_bf16_f32 v163, v100, v101
	v_cvt_pk_bf16_f32 v164, v106, v107
	v_cvt_pk_bf16_f32 v165, v108, v109
	ds_write2st64_b64 v154, v[170:171], v[172:173] offset1:1
	ds_write2st64_b64 v154, v[162:163], v[164:165] offset0:2 offset1:3
	s_nop 1
	v_mov_b32_e32 v222, s9
	v_add_u32_e32 v222, 0x10000, v222
	v_mov_b32_e32 v223, s14
	s_waitcnt vmcnt(37)
	v_lshlrev_b32_e32 v154, 16, v212
	v_and_b32_e32 v155, 0xffff0000, v212
	v_pk_fma_f32 v[150:151], v[166:167], v[150:151], v[154:155]
	v_lshlrev_b32_e32 v154, 16, v213
	v_and_b32_e32 v155, 0xffff0000, v213
	v_pk_fma_f32 v[152:153], v[168:169], v[152:153], v[154:155]
	s_cmpk_lt_u32 s20, 0x78
	s_nop 0
	v_mfma_f32_16x16x32_bf16 v[150:153], v[158:161], v[170:173], v[150:153]
	v_mfma_f32_16x16x32_bf16 v[154:157], v[146:149], v[162:165], v[150:153]
	s_waitcnt lgkmcnt(0)
	s_mov_b64 s[98:99], exec
	s_mov_b64 exec, s[0:1]
	ds_write_b32 v222, v223
	s_mov_b64 exec, s[98:99]
	s_waitcnt vmcnt(36)
	v_lshlrev_b32_e32 v146, 16, v208
	v_and_b32_e32 v147, 0xffff0000, v208
	v_pk_fma_f32 v[102:103], v[142:143], v[102:103], v[146:147]
	v_lshlrev_b32_e32 v142, 16, v209
	v_and_b32_e32 v143, 0xffff0000, v209
	v_pk_fma_f32 v[104:105], v[144:145], v[104:105], v[142:143]
	s_nop 1
	v_mfma_f32_16x16x32_bf16 v[102:105], v[130:133], v[170:173], v[102:105]
	v_mfma_f32_16x16x32_bf16 v[150:153], v[134:137], v[162:165], v[102:105]
	s_waitcnt vmcnt(35)
	s_nop 5
	v_lshlrev_b32_e32 v102, 16, v206
	v_and_b32_e32 v103, 0xffff0000, v206
	s_waitcnt vmcnt(33)
	v_pk_fma_f32 v[98:99], v[138:139], v[98:99], v[102:103]
	v_lshlrev_b32_e32 v102, 16, v207
	v_and_b32_e32 v103, 0xffff0000, v207
	v_pk_fma_f32 v[100:101], v[140:141], v[100:101], v[102:103]
	s_nop 1
	v_mfma_f32_16x16x32_bf16 v[98:101], v[122:125], v[170:173], v[98:101]
	v_mfma_f32_16x16x32_bf16 v[102:105], v[126:129], v[162:165], v[98:101]
	s_nop 6
	v_lshlrev_b32_e32 v98, 16, v180
	v_and_b32_e32 v99, 0xffff0000, v180
	v_lshlrev_b32_e32 v100, 16, v181
	v_and_b32_e32 v101, 0xffff0000, v181
	s_waitcnt vmcnt(32)
	v_pk_fma_f32 v[98:99], v[118:119], v[106:107], v[98:99]
	v_pk_fma_f32 v[100:101], v[120:121], v[108:109], v[100:101]
	s_nop 1
	v_mfma_f32_16x16x32_bf16 v[98:101], v[114:117], v[170:173], v[98:101]
	v_mfma_f32_16x16x32_bf16 v[106:109], v[110:113], v[162:165], v[98:101]
	s_cbranch_scc0 .LBB0_3652
	s_mov_b32 s20, s14
	s_branch .LBB0_3620
